# final-norm gain prefetch issued before the row reduction instead of after it
# baseline (speedup 1.0000x reference)
; DEVI float bflo(unsigned w) { return __uint_as_float(w << 16); }
; DEVI float bfhi(unsigned w) { return __uint_as_float(w & 0xffff0000u); }
; template <int MODE>
; DEVI void phase_rows(const Params& p, int l, char* smem) {
;     ...
;             {   u32x2 w0[8], w1[8], w2[8], w3[8];
; #pragma unroll
;                 for (int i = 0; i < 8; ++i) { w0[i] = *(const u32x2*)(y0 + i * 256 + lane * 4); w1[i] = *(const u32x2*)(y1 + i * 256 + lane * 4);
;                     w2[i] = *(const u32x2*)(y2 + i * 256 + lane * 4); w3[i] = *(const u32x2*)(y3 + i * 256 + lane * 4); }
;                 const float f0 = ny > 0 ? 1.f : 0.f, f1 = ny > 1 ? 1.f : 0.f, f2 = ny > 2 ? 1.f : 0.f, f3 = ny > 3 ? 1.f : 0.f;
; #pragma unroll
;                 for (int i = 0; i < 8; ++i) {
;                     cacc[i * 4] += f0 * bflo(w0[i][0]) + f1 * bflo(w1[i][0]) + f2 * bflo(w2[i][0]) + f3 * bflo(w3[i][0]);
;                     cacc[i * 4 + 1] += f0 * bfhi(w0[i][0]) + f1 * bfhi(w1[i][0]) + f2 * bfhi(w2[i][0]) + f3 * bfhi(w3[i][0]);
;                     cacc[i * 4 + 2] += f0 * bflo(w0[i][1]) + f1 * bflo(w1[i][1]) + f2 * bflo(w2[i][1]) + f3 * bflo(w3[i][1]);
;                     cacc[i * 4 + 3] += f0 * bfhi(w0[i][1]) + f1 * bfhi(w1[i][1]) + f2 * bfhi(w2[i][1]) + f3 * bfhi(w3[i][1]); }
;             }
;             const float* gf = mrow + 10240;
; #pragma unroll
;             for (int i = 0; i < 8; ++i) { const f32x4 g = *(const f32x4*)(gf + i * 256 + lane * 4);
.LBB0_1467:
	s_or_b64 exec, exec, s[16:17]
	v_lshlrev_b32_e32 v2, 1, v50
	v_lshl_add_u64 v[96:97], v[78:79], 0, v[2:3]
	v_lshl_add_u64 v[98:99], v[74:75], 0, v[2:3]
	global_load_dwordx2 v[106:107], v[96:97], off
	global_load_dwordx2 v[108:109], v[98:99], off
	global_load_dwordx2 v[120:121], v[96:97], off offset:512
	global_load_dwordx2 v[122:123], v[98:99], off offset:512
	v_lshlrev_b32_e32 v104, 16, v46
	v_and_b32_e32 v105, 0xffff0000, v46
	v_lshlrev_b32_e32 v102, 16, v47
	v_and_b32_e32 v103, 0xffff0000, v47
	global_load_dwordx2 v[46:47], v[96:97], off offset:1024
	global_load_dwordx2 v[126:127], v[98:99], off offset:1024
	v_mul_hi_i32_i24_e32 v113, 0xc000, v49
	v_mul_i32_i24_e32 v112, 0xc000, v49
	v_lshlrev_b32_e32 v100, 16, v70
	v_and_b32_e32 v101, 0xffff0000, v70
	v_lshlrev_b32_e32 v110, 16, v71
	v_and_b32_e32 v111, 0xffff0000, v71
	v_lshlrev_b32_e32 v124, 16, v68
	v_and_b32_e32 v125, 0xffff0000, v68
	v_lshlrev_b32_e32 v118, 16, v69
	v_and_b32_e32 v119, 0xffff0000, v69
	v_lshlrev_b32_e32 v94, 16, v44
	v_and_b32_e32 v95, 0xffff0000, v44
	v_lshlrev_b32_e32 v92, 16, v45
	v_and_b32_e32 v93, 0xffff0000, v45
	v_lshlrev_b32_e32 v90, 16, v42
	v_and_b32_e32 v91, 0xffff0000, v42
	global_load_dwordx2 v[44:45], v[96:97], off offset:1536
	global_load_dwordx2 v[128:129], v[98:99], off offset:1536
	v_lshlrev_b32_e32 v88, 16, v43
	v_and_b32_e32 v89, 0xffff0000, v43
	v_lshlrev_b32_e32 v86, 16, v40
	v_and_b32_e32 v87, 0xffff0000, v40
	v_lshlrev_b32_e32 v84, 16, v41
	v_and_b32_e32 v85, 0xffff0000, v41
	v_lshlrev_b32_e32 v82, 16, v38
	v_and_b32_e32 v83, 0xffff0000, v38
	global_load_dwordx2 v[40:41], v[96:97], off offset:2048
	global_load_dwordx2 v[42:43], v[98:99], off offset:2048
	v_lshlrev_b32_e32 v80, 16, v39
	v_and_b32_e32 v81, 0xffff0000, v39
	v_lshlrev_b32_e32 v70, 16, v36
	v_and_b32_e32 v71, 0xffff0000, v36
	v_lshlrev_b32_e32 v68, 16, v37
	v_and_b32_e32 v69, 0xffff0000, v37
	global_load_dwordx2 v[36:37], v[96:97], off offset:2560
	global_load_dwordx2 v[38:39], v[98:99], off offset:2560
	v_cmp_lt_u32_e32 vcc, 2, v116
	v_lshl_add_u64 v[72:73], v[72:73], 0, v[2:3]
	v_lshl_add_u64 v[76:77], v[76:77], 0, v[2:3]
	v_lshl_add_u64 v[134:135], s[82:83], 0, v[112:113]
	v_lshlrev_b32_e32 v2, 2, v50
	v_cndmask_b32_e64 v74, 0, 1.0, vcc
	v_cmp_lt_u32_e32 vcc, 3, v116
	v_lshl_add_u64 v[134:135], v[134:135], 0, v[2:3]
	global_load_dwordx2 v[138:139], v[96:97], off offset:3072
	global_load_dwordx2 v[144:145], v[98:99], off offset:3072
	v_cndmask_b32_e64 v78, 0, 1.0, vcc
	v_add_co_u32_e32 v202, vcc, s62, v134
	global_load_dwordx2 v[180:181], v[96:97], off offset:3584
	global_load_dwordx2 v[182:183], v[98:99], off offset:3584
	global_load_dwordx2 v[184:185], v[72:73], off
	global_load_dwordx2 v[188:189], v[72:73], off offset:512
	global_load_dwordx2 v[190:191], v[72:73], off offset:1024
	global_load_dwordx2 v[150:151], v[72:73], off offset:1536
	global_load_dwordx2 v[186:187], v[76:77], off
	global_load_dwordx2 v[192:193], v[76:77], off offset:512
	global_load_dwordx2 v[194:195], v[76:77], off offset:1024
	global_load_dwordx2 v[152:153], v[76:77], off offset:1536
	global_load_dwordx2 v[130:131], v[72:73], off offset:2048
	global_load_dwordx2 v[112:113], v[72:73], off offset:2560
	global_load_dwordx2 v[96:97], v[72:73], off offset:3072
	s_nop 0
	global_load_dwordx2 v[72:73], v[72:73], off offset:3584
	s_nop 0
	global_load_dwordx2 v[132:133], v[76:77], off offset:2048
	global_load_dwordx2 v[114:115], v[76:77], off offset:2560
	global_load_dwordx2 v[98:99], v[76:77], off offset:3072
	s_nop 0
	global_load_dwordx2 v[76:77], v[76:77], off offset:3584
	v_addc_co_u32_e32 v203, vcc, 0, v135, vcc
	global_load_dwordx4 v[168:171], v[202:203], off offset:-4096
	s_mov_b64 s[4:5], 0xe000
	v_cmp_eq_u32_e32 vcc, 0, v116
	v_add_u32_e32 v48, s44, v48
	s_waitcnt vmcnt(32)
	v_lshlrev_b32_e32 v198, 16, v106
	v_cndmask_b32_e64 v117, 1.0, 0, vcc
	v_cmp_lt_u32_e32 vcc, 1, v116
	s_waitcnt vmcnt(31)
	v_and_b32_e32 v199, 0xffff0000, v108
	v_lshlrev_b32_e32 v200, 16, v108
	v_cndmask_b32_e64 v116, 0, 1.0, vcc
	s_waitcnt vmcnt(28)
	v_lshlrev_b32_e32 v216, 16, v46
	v_and_b32_e32 v219, 0xffff0000, v46
	v_lshlrev_b32_e32 v220, 16, v47
	v_and_b32_e32 v229, 0xffff0000, v47
	v_lshl_add_u64 v[46:47], v[134:135], 0, s[4:5]
	global_load_dwordx4 v[172:175], v[46:47], off offset:1024
	global_load_dwordx4 v[176:179], v[46:47], off offset:2048
	v_and_b32_e32 v201, 0xffff0000, v106
	v_lshlrev_b32_e32 v204, 16, v107
	v_lshlrev_b32_e32 v206, 16, v109
	v_and_b32_e32 v207, 0xffff0000, v107
	v_and_b32_e32 v205, 0xffff0000, v109
	v_lshlrev_b32_e32 v208, 16, v120
	v_lshlrev_b32_e32 v210, 16, v122
	v_and_b32_e32 v211, 0xffff0000, v120
	v_and_b32_e32 v209, 0xffff0000, v122
	v_lshlrev_b32_e32 v212, 16, v121
	v_lshlrev_b32_e32 v214, 16, v123
	v_and_b32_e32 v215, 0xffff0000, v121
	v_and_b32_e32 v213, 0xffff0000, v123
	s_waitcnt vmcnt(28)
	v_lshlrev_b32_e32 v232, 16, v44
	v_and_b32_e32 v237, 0xffff0000, v44
	v_lshlrev_b32_e32 v240, 16, v45
	v_and_b32_e32 v243, 0xffff0000, v45
	v_lshlrev_b32_e32 v228, 16, v127
	v_and_b32_e32 v221, 0xffff0000, v127
	s_waitcnt vmcnt(26)
	v_lshlrev_b32_e32 v158, 16, v40
	s_waitcnt vmcnt(25)
	v_lshlrev_b32_e32 v160, 16, v42
	v_and_b32_e32 v161, 0xffff0000, v40
	v_and_b32_e32 v159, 0xffff0000, v42
	s_waitcnt vmcnt(20)
	v_lshlrev_b32_e32 v120, 16, v180
	s_waitcnt vmcnt(19)
; DEVI float bflo(unsigned w) { return __uint_as_float(w << 16); }
; DEVI float bfhi(unsigned w) { return __uint_as_float(w & 0xffff0000u); }
; template <int MODE>
; DEVI void phase_rows(const Params& p, int l, char* smem) {
;     ...
;                 for (int i = 0; i < 8; ++i) { w0[i] = *(const u32x2*)(y0 + i * 256 + lane * 4); w1[i] = *(const u32x2*)(y1 + i * 256 + lane * 4);
;                     w2[i] = *(const u32x2*)(y2 + i * 256 + lane * 4); w3[i] = *(const u32x2*)(y3 + i * 256 + lane * 4); }
;                 const float f0 = ny > 0 ? 1.f : 0.f, f1 = ny > 1 ? 1.f : 0.f, f2 = ny > 2 ? 1.f : 0.f, f3 = ny > 3 ? 1.f : 0.f;
; #pragma unroll
;                 for (int i = 0; i < 8; ++i) {
;                     cacc[i * 4] += f0 * bflo(w0[i][0]) + f1 * bflo(w1[i][0]) + f2 * bflo(w2[i][0]) + f3 * bflo(w3[i][0]);
;                     cacc[i * 4 + 1] += f0 * bfhi(w0[i][0]) + f1 * bfhi(w1[i][0]) + f2 * bfhi(w2[i][0]) + f3 * bfhi(w3[i][0]);
;                     cacc[i * 4 + 2] += f0 * bflo(w0[i][1]) + f1 * bflo(w1[i][1]) + f2 * bflo(w2[i][1]) + f3 * bflo(w3[i][1]);
;                     cacc[i * 4 + 3] += f0 * bfhi(w0[i][1]) + f1 * bfhi(w1[i][1]) + f2 * bfhi(w2[i][1]) + f3 * bfhi(w3[i][1]); }
;             }
;             const float* gf = mrow + 10240;
; #pragma unroll
;             for (int i = 0; i < 8; ++i) { const f32x4 g = *(const f32x4*)(gf + i * 256 + lane * 4);
;                 v[i * 4] += g[0] * cacc[i * 4]; v[i * 4 + 1] += g[1] * cacc[i * 4 + 1]; v[i * 4 + 2] += g[2] * cacc[i * 4 + 2]; v[i * 4 + 3] += g[3] * cacc[i * 4 + 3]; }
	v_lshlrev_b32_e32 v122, 16, v182
	v_and_b32_e32 v123, 0xffff0000, v180
	v_lshlrev_b32_e32 v146, 16, v36
	v_and_b32_e32 v149, 0xffff0000, v36
	v_lshlrev_b32_e32 v140, 16, v37
	v_and_b32_e32 v143, 0xffff0000, v37
	v_and_b32_e32 v121, 0xffff0000, v182
	v_lshlrev_b32_e32 v106, 16, v181
	v_lshlrev_b32_e32 v108, 16, v183
	v_and_b32_e32 v109, 0xffff0000, v181
	v_and_b32_e32 v107, 0xffff0000, v183
	global_load_dwordx4 v[180:183], v[46:47], off offset:3072
	v_pk_mul_f32 v[36:37], v[116:117], v[198:199] op_sel:[1,0] op_sel_hi:[0,1]
	v_lshlrev_b32_e32 v148, 16, v38
	v_and_b32_e32 v147, 0xffff0000, v38
	v_lshlrev_b32_e32 v142, 16, v39
	v_and_b32_e32 v141, 0xffff0000, v39
	v_pk_fma_f32 v[36:37], v[116:117], v[200:201], v[36:37]
	s_waitcnt vmcnt(19)
	v_lshlrev_b32_e32 v38, 16, v184
	v_and_b32_e32 v39, 0xffff0000, v184
	v_pk_fma_f32 v[36:37], v[74:75], v[38:39], v[36:37] op_sel_hi:[0,1,1]
	s_waitcnt vmcnt(15)
	v_lshlrev_b32_e32 v38, 16, v186
	v_and_b32_e32 v39, 0xffff0000, v186
	v_pk_fma_f32 v[36:37], v[78:79], v[38:39], v[36:37] op_sel_hi:[0,1,1]
	v_pk_add_f32 v[4:5], v[4:5], v[36:37]
	v_lshlrev_b32_e32 v36, 16, v187
	s_waitcnt vmcnt(3)
	v_pk_fma_f32 v[100:101], v[4:5], v[168:169], v[100:101]
	v_lshlrev_b32_e32 v4, 16, v185
	v_and_b32_e32 v5, 0xffff0000, v185
	v_and_b32_e32 v37, 0xffff0000, v187
	global_load_dwordx4 v[184:187], v[202:203], off
	global_load_dwordx4 v[44:47], v[202:203], off offset:1024
	v_pk_mul_f32 v[38:39], v[116:117], v[204:205] op_sel:[1,0] op_sel_hi:[0,1]
	v_pk_fma_f32 v[38:39], v[116:117], v[206:207], v[38:39]
	v_lshlrev_b32_e32 v154, 16, v41
	v_pk_fma_f32 v[4:5], v[74:75], v[4:5], v[38:39] op_sel_hi:[0,1,1]
	v_lshlrev_b32_e32 v156, 16, v43
	v_and_b32_e32 v157, 0xffff0000, v41
	v_and_b32_e32 v155, 0xffff0000, v43
	v_pk_fma_f32 v[4:5], v[78:79], v[36:37], v[4:5] op_sel_hi:[0,1,1]
	global_load_dwordx4 v[40:43], v[202:203], off offset:2048
	global_load_dwordx4 v[36:39], v[202:203], off offset:3072
	v_lshlrev_b32_e32 v236, 16, v128
	v_and_b32_e32 v233, 0xffff0000, v128
	v_lshlrev_b32_e32 v136, 16, v144
	v_and_b32_e32 v135, 0xffff0000, v144
	v_lshlrev_b32_e32 v128, 16, v145
	v_and_b32_e32 v127, 0xffff0000, v145
	v_pk_mul_f32 v[144:145], v[116:117], v[208:209] op_sel:[1,0] op_sel_hi:[0,1]
	v_pk_fma_f32 v[144:145], v[116:117], v[210:211], v[144:145]
	v_lshlrev_b32_e32 v168, 16, v188
	v_and_b32_e32 v169, 0xffff0000, v188
	v_pk_fma_f32 v[144:145], v[74:75], v[168:169], v[144:145] op_sel_hi:[0,1,1]
	v_lshlrev_b32_e32 v168, 16, v192
	v_and_b32_e32 v169, 0xffff0000, v192
	v_pk_fma_f32 v[168:169], v[78:79], v[168:169], v[144:145] op_sel_hi:[0,1,1]
	v_pk_add_f32 v[8:9], v[8:9], v[168:169]
	v_pk_add_f32 v[4:5], v[6:7], v[4:5]
	s_waitcnt vmcnt(6)
	v_pk_fma_f32 v[8:9], v[8:9], v[172:173], v[124:125]
	v_pk_mul_f32 v[172:173], v[116:117], v[212:213] op_sel:[1,0] op_sel_hi:[0,1]
	v_lshlrev_b32_e32 v168, 16, v189
	v_and_b32_e32 v169, 0xffff0000, v189
	v_pk_fma_f32 v[172:173], v[116:117], v[214:215], v[172:173]
	v_and_b32_e32 v217, 0xffff0000, v126
	v_pk_fma_f32 v[110:111], v[4:5], v[170:171], v[110:111]
	v_lshlrev_b32_e32 v170, 16, v193
	v_and_b32_e32 v171, 0xffff0000, v193
	v_pk_fma_f32 v[168:169], v[74:75], v[168:169], v[172:173] op_sel_hi:[0,1,1]
	v_lshlrev_b32_e32 v218, 16, v126
	v_pk_fma_f32 v[168:169], v[78:79], v[170:171], v[168:169] op_sel_hi:[0,1,1]
	v_pk_mul_f32 v[172:173], v[116:117], v[216:217] op_sel:[1,0] op_sel_hi:[0,1]
	v_pk_add_f32 v[10:11], v[10:11], v[168:169]
	v_lshlrev_b32_e32 v168, 16, v190
	v_and_b32_e32 v169, 0xffff0000, v190
	v_pk_fma_f32 v[172:173], v[116:117], v[218:219], v[172:173]
	v_lshlrev_b32_e32 v170, 16, v194
	v_and_b32_e32 v171, 0xffff0000, v194
	v_pk_fma_f32 v[168:169], v[74:75], v[168:169], v[172:173] op_sel_hi:[0,1,1]
	v_pk_fma_f32 v[168:169], v[78:79], v[170:171], v[168:169] op_sel_hi:[0,1,1]
	v_pk_mul_f32 v[172:173], v[116:117], v[220:221] op_sel:[1,0] op_sel_hi:[0,1]
	v_pk_add_f32 v[12:13], v[12:13], v[168:169]
	v_lshlrev_b32_e32 v168, 16, v191
	v_and_b32_e32 v169, 0xffff0000, v191
	v_pk_fma_f32 v[172:173], v[116:117], v[228:229], v[172:173]
	v_lshlrev_b32_e32 v170, 16, v195
	v_and_b32_e32 v171, 0xffff0000, v195
	v_pk_fma_f32 v[168:169], v[74:75], v[168:169], v[172:173] op_sel_hi:[0,1,1]
	v_pk_fma_f32 v[168:169], v[78:79], v[170:171], v[168:169] op_sel_hi:[0,1,1]
	v_pk_mul_f32 v[172:173], v[116:117], v[232:233] op_sel:[1,0] op_sel_hi:[0,1]
	v_pk_add_f32 v[14:15], v[14:15], v[168:169]
	v_lshlrev_b32_e32 v168, 16, v150
	v_and_b32_e32 v169, 0xffff0000, v150
	v_pk_fma_f32 v[172:173], v[116:117], v[236:237], v[172:173]
	v_lshlrev_b32_e32 v170, 16, v152
	v_and_b32_e32 v171, 0xffff0000, v152
	v_pk_fma_f32 v[168:169], v[74:75], v[168:169], v[172:173] op_sel_hi:[0,1,1]
	v_and_b32_e32 v241, 0xffff0000, v129
	v_pk_fma_f32 v[168:169], v[78:79], v[170:171], v[168:169] op_sel_hi:[0,1,1]
	v_lshlrev_b32_e32 v242, 16, v129
	v_pk_add_f32 v[16:17], v[16:17], v[168:169]
	v_pk_mul_f32 v[168:169], v[116:117], v[240:241] op_sel:[1,0] op_sel_hi:[0,1]
	v_lshlrev_b32_e32 v150, 16, v151
	v_and_b32_e32 v151, 0xffff0000, v151
	v_pk_fma_f32 v[168:169], v[116:117], v[242:243], v[168:169]
	v_lshlrev_b32_e32 v152, 16, v153
	v_and_b32_e32 v153, 0xffff0000, v153
	v_pk_fma_f32 v[150:151], v[74:75], v[150:151], v[168:169] op_sel_hi:[0,1,1]
	v_pk_fma_f32 v[150:151], v[78:79], v[152:153], v[150:151] op_sel_hi:[0,1,1]
	v_pk_add_f32 v[18:19], v[18:19], v[150:151]
	v_pk_mul_f32 v[158:159], v[116:117], v[158:159] op_sel:[1,0] op_sel_hi:[0,1]
	s_waitcnt vmcnt(4)
; DEVI unsigned cvt_pk(float lo, float hi) { f32x2 v = {lo, hi}; bf16x2_t b = __builtin_convertvector(v, bf16x2_t); return __builtin_bit_cast(unsigned, b); }
; template <int MODE>
; DEVI void phase_rows(const Params& p, int l, char* smem) {
;     ...
;             for (int i = 0; i < 8; ++i) { const f32x4 g = *(const f32x4*)(gf + i * 256 + lane * 4);
;                 v[i * 4] += g[0] * cacc[i * 4]; v[i * 4 + 1] += g[1] * cacc[i * 4 + 1]; v[i * 4 + 2] += g[2] * cacc[i * 4 + 2]; v[i * 4 + 3] += g[3] * cacc[i * 4 + 3]; }
;             if (MODE == 2) {
; #pragma unroll
;                 for (int i = 0; i < 8; ++i) *(u32x2*)(xres + (size_t)row * DM + i * 256 + lane * 4) = (u32x2){cvt_pk(v[i * 4], v[i * 4 + 1]), cvt_pk(v[i * 4 + 2], v[i * 4 + 3])};
;             }
;         }
;         f32x4 shv[8], scv[8];
;         if (MODE != 3) { const float* mr2 = (MODE == 2) ? mrow + (size_t)5 * 12288 : mrow;
;             const float* sh = mr2 + ((MODE == 1) ? 6144 : 0); const float* sc = mr2 + ((MODE == 1) ? 8192 : 2048);
; #pragma unroll
;             for (int i = 0; i < 8; ++i) { shv[i] = *(const f32x4*)(sh + i * 256 + lane * 4); scv[i] = *(const f32x4*)(sc + i * 256 + lane * 4); } }
;         float ss = 0.f;
; #pragma unroll
;         for (int i = 0; i < 32; ++i) ss += v[i] * v[i];
;         ss = wave_sum(ss);
;         const float rstd = rsqrtf(ss * (1.f / DM) + EPS);
;         if (MODE == 3) {
; #pragma unroll
;             for (int i = 0; i < 8; ++i) { const f32x4 g = *(const f32x4*)(p.final_norm + i * 256 + lane * 4);
;                 __builtin_nontemporal_store((f32x4){v[i * 4] * rstd * g[0], v[i * 4 + 1] * rstd * g[1], v[i * 4 + 2] * rstd * g[2], v[i * 4 + 3] * rstd * g[3]}, (f32x4*)(p.out + (size_t)row * DM + i * 256 + lane * 4)); }
	v_pk_fma_f32 v[92:93], v[18:19], v[182:183], v[92:93]
	v_lshlrev_b32_e32 v18, 16, v130
	v_and_b32_e32 v19, 0xffff0000, v130
	v_pk_fma_f32 v[158:159], v[116:117], v[160:161], v[158:159]
	v_lshlrev_b32_e32 v152, 16, v132
	v_and_b32_e32 v153, 0xffff0000, v132
	v_pk_fma_f32 v[18:19], v[74:75], v[18:19], v[158:159] op_sel_hi:[0,1,1]
	v_pk_fma_f32 v[18:19], v[78:79], v[152:153], v[18:19] op_sel_hi:[0,1,1]
	v_pk_add_f32 v[18:19], v[20:21], v[18:19]
	global_load_dwordx4 v[4:7], v[54:55], off
	global_load_dwordx4 v[198:201], v[54:55], off offset:1024
	global_load_dwordx4 v[202:205], v[54:55], off offset:2048
	global_load_dwordx4 v[206:209], v[54:55], off offset:3072
	global_load_dwordx4 v[210:213], v[58:59], off
	global_load_dwordx4 v[214:217], v[60:61], off
	global_load_dwordx4 v[218:221], v[62:63], off
	global_load_dwordx4 v[168:171], v[64:65], off
	s_waitcnt vmcnt(11)
	v_pk_fma_f32 v[18:19], v[18:19], v[184:185], v[90:91]
	v_lshlrev_b32_e32 v90, 16, v131
	v_and_b32_e32 v91, 0xffff0000, v131
	v_lshlrev_b32_e32 v130, 16, v133
	v_and_b32_e32 v131, 0xffff0000, v133
	v_pk_mul_f32 v[132:133], v[116:117], v[154:155] op_sel:[1,0] op_sel_hi:[0,1]
	v_pk_fma_f32 v[132:133], v[116:117], v[156:157], v[132:133]
	v_lshlrev_b32_e32 v134, 16, v138
	v_and_b32_e32 v137, 0xffff0000, v138
	v_lshlrev_b32_e32 v126, 16, v139
	v_and_b32_e32 v129, 0xffff0000, v139
	v_pk_mul_f32 v[138:139], v[100:101], v[100:101]
	v_pk_fma_f32 v[90:91], v[74:75], v[90:91], v[132:133] op_sel_hi:[0,1,1]
	v_pk_mul_f32 v[144:145], v[110:111], v[110:111]
	v_pk_fma_f32 v[90:91], v[78:79], v[130:131], v[90:91] op_sel_hi:[0,1,1]
	v_pk_mul_f32 v[132:133], v[116:117], v[146:147] op_sel:[1,0] op_sel_hi:[0,1]
	v_add_f32_e32 v1, v138, v139
	v_pk_add_f32 v[22:23], v[22:23], v[90:91]
	v_lshlrev_b32_e32 v90, 16, v112
	v_and_b32_e32 v91, 0xffff0000, v112
	v_pk_fma_f32 v[132:133], v[116:117], v[148:149], v[132:133]
	v_add_f32_e32 v1, v144, v1
	v_pk_mul_f32 v[124:125], v[8:9], v[8:9]
	v_lshlrev_b32_e32 v130, 16, v114
	v_and_b32_e32 v131, 0xffff0000, v114
	v_pk_fma_f32 v[90:91], v[74:75], v[90:91], v[132:133] op_sel_hi:[0,1,1]
	v_add_f32_e32 v1, v145, v1
	v_pk_fma_f32 v[10:11], v[10:11], v[174:175], v[118:119]
	v_pk_fma_f32 v[90:91], v[78:79], v[130:131], v[90:91] op_sel_hi:[0,1,1]
	v_add_f32_e32 v1, v124, v1
	v_pk_mul_f32 v[118:119], v[10:11], v[10:11]
	v_pk_add_f32 v[24:25], v[24:25], v[90:91]
	v_add_f32_e32 v1, v125, v1
	v_pk_fma_f32 v[12:13], v[12:13], v[176:177], v[104:105]
	s_waitcnt vmcnt(10)
	v_pk_fma_f32 v[24:25], v[24:25], v[44:45], v[86:87]
	v_lshlrev_b32_e32 v86, 16, v113
	v_and_b32_e32 v87, 0xffff0000, v113
	v_pk_mul_f32 v[112:113], v[116:117], v[140:141] op_sel:[1,0] op_sel_hi:[0,1]
	v_add_f32_e32 v1, v118, v1
	v_pk_mul_f32 v[104:105], v[12:13], v[12:13]
	v_pk_fma_f32 v[112:113], v[116:117], v[142:143], v[112:113]
	v_add_f32_e32 v1, v119, v1
	v_pk_fma_f32 v[14:15], v[14:15], v[178:179], v[102:103]
	v_lshlrev_b32_e32 v90, 16, v115
	v_and_b32_e32 v91, 0xffff0000, v115
	v_pk_fma_f32 v[86:87], v[74:75], v[86:87], v[112:113] op_sel_hi:[0,1,1]
	v_add_f32_e32 v1, v104, v1
	v_pk_mul_f32 v[102:103], v[14:15], v[14:15]
	v_pk_fma_f32 v[86:87], v[78:79], v[90:91], v[86:87] op_sel_hi:[0,1,1]
	v_add_f32_e32 v1, v105, v1
	v_pk_fma_f32 v[16:17], v[16:17], v[180:181], v[94:95]
	v_pk_add_f32 v[26:27], v[26:27], v[86:87]
	v_pk_mul_f32 v[90:91], v[116:117], v[134:135] op_sel:[1,0] op_sel_hi:[0,1]
	v_add_f32_e32 v1, v102, v1
	v_pk_mul_f32 v[94:95], v[16:17], v[16:17]
	v_pk_fma_f32 v[26:27], v[26:27], v[46:47], v[84:85]
	v_lshlrev_b32_e32 v84, 16, v96
	v_and_b32_e32 v85, 0xffff0000, v96
	v_pk_fma_f32 v[90:91], v[116:117], v[136:137], v[90:91]
	v_add_f32_e32 v1, v103, v1
	v_lshlrev_b32_e32 v86, 16, v98
	v_and_b32_e32 v87, 0xffff0000, v98
	v_pk_fma_f32 v[84:85], v[74:75], v[84:85], v[90:91] op_sel_hi:[0,1,1]
	v_add_f32_e32 v1, v94, v1
	v_pk_mul_f32 v[150:151], v[92:93], v[92:93]
	v_pk_fma_f32 v[84:85], v[78:79], v[86:87], v[84:85] op_sel_hi:[0,1,1]
	v_add_f32_e32 v1, v95, v1
	v_pk_add_f32 v[28:29], v[28:29], v[84:85]
	v_pk_mul_f32 v[86:87], v[116:117], v[126:127] op_sel:[1,0] op_sel_hi:[0,1]
	v_add_f32_e32 v1, v150, v1
	v_pk_mul_f32 v[20:21], v[18:19], v[18:19]
	s_waitcnt vmcnt(9)
	v_pk_fma_f32 v[28:29], v[28:29], v[40:41], v[82:83]
	v_lshlrev_b32_e32 v82, 16, v97
	v_and_b32_e32 v83, 0xffff0000, v97
	v_pk_fma_f32 v[86:87], v[116:117], v[128:129], v[86:87]
	v_add_f32_e32 v1, v151, v1
	v_pk_fma_f32 v[22:23], v[22:23], v[186:187], v[88:89]
	v_lshlrev_b32_e32 v84, 16, v99
	v_and_b32_e32 v85, 0xffff0000, v99
	v_pk_fma_f32 v[82:83], v[74:75], v[82:83], v[86:87] op_sel_hi:[0,1,1]
	v_add_f32_e32 v1, v20, v1
	v_pk_mul_f32 v[88:89], v[22:23], v[22:23]
	v_pk_fma_f32 v[82:83], v[78:79], v[84:85], v[82:83] op_sel_hi:[0,1,1]
	v_add_f32_e32 v1, v21, v1
	v_pk_add_f32 v[30:31], v[30:31], v[82:83]
	v_pk_mul_f32 v[84:85], v[116:117], v[120:121] op_sel:[1,0] op_sel_hi:[0,1]
	v_add_f32_e32 v1, v88, v1
	v_pk_mul_f32 v[44:45], v[24:25], v[24:25]
	v_pk_fma_f32 v[30:31], v[30:31], v[42:43], v[80:81]
	v_lshlrev_b32_e32 v80, 16, v72
	v_and_b32_e32 v81, 0xffff0000, v72
	v_pk_fma_f32 v[84:85], v[116:117], v[122:123], v[84:85]
	v_add_f32_e32 v1, v89, v1
	v_lshlrev_b32_e32 v82, 16, v76
	v_and_b32_e32 v83, 0xffff0000, v76
	v_pk_fma_f32 v[80:81], v[74:75], v[80:81], v[84:85] op_sel_hi:[0,1,1]
	v_add_f32_e32 v1, v44, v1
	v_pk_mul_f32 v[46:47], v[26:27], v[26:27]
	v_pk_fma_f32 v[80:81], v[78:79], v[82:83], v[80:81] op_sel_hi:[0,1,1]
	v_add_f32_e32 v1, v45, v1
	v_pk_add_f32 v[32:33], v[32:33], v[80:81]
	v_add_f32_e32 v1, v46, v1
	v_pk_mul_f32 v[40:41], v[28:29], v[28:29]
	s_waitcnt vmcnt(8)
; template <int MODE>
; DEVI void phase_rows(const Params& p, int l, char* smem) {
;     ...
;         float ss = 0.f;
; #pragma unroll
;         for (int i = 0; i < 32; ++i) ss += v[i] * v[i];
;         ss = wave_sum(ss);
;         const float rstd = rsqrtf(ss * (1.f / DM) + EPS);
;         if (MODE == 3) {
; #pragma unroll
;             for (int i = 0; i < 8; ++i) { const f32x4 g = *(const f32x4*)(p.final_norm + i * 256 + lane * 4);
;                 __builtin_nontemporal_store((f32x4){v[i * 4] * rstd * g[0], v[i * 4 + 1] * rstd * g[1], v[i * 4 + 2] * rstd * g[2], v[i * 4 + 3] * rstd * g[3]}, (f32x4*)(p.out + (size_t)row * DM + i * 256 + lane * 4)); }
;             continue;
	v_pk_fma_f32 v[32:33], v[32:33], v[36:37], v[70:71]
	v_lshlrev_b32_e32 v70, 16, v73
	v_and_b32_e32 v71, 0xffff0000, v73
	v_lshlrev_b32_e32 v72, 16, v77
	v_and_b32_e32 v73, 0xffff0000, v77
	v_pk_mul_f32 v[76:77], v[116:117], v[106:107] op_sel:[1,0] op_sel_hi:[0,1]
	v_add_f32_e32 v1, v47, v1
	v_pk_fma_f32 v[76:77], v[116:117], v[108:109], v[76:77]
	v_add_f32_e32 v1, v40, v1
	v_pk_mul_f32 v[42:43], v[30:31], v[30:31]
	v_pk_fma_f32 v[70:71], v[74:75], v[70:71], v[76:77] op_sel_hi:[0,1,1]
	v_add_f32_e32 v1, v41, v1
	v_pk_fma_f32 v[70:71], v[78:79], v[72:73], v[70:71] op_sel_hi:[0,1,1]
	v_add_f32_e32 v1, v42, v1
	v_pk_mul_f32 v[36:37], v[32:33], v[32:33]
	v_pk_add_f32 v[34:35], v[34:35], v[70:71]
	v_add_f32_e32 v1, v43, v1
	v_pk_fma_f32 v[34:35], v[34:35], v[38:39], v[68:69]
	v_add_f32_e32 v1, v36, v1
	v_pk_mul_f32 v[38:39], v[34:35], v[34:35]
	v_add_f32_e32 v1, v37, v1
	v_add_f32_e32 v1, v38, v1
	v_add_f32_e32 v1, v39, v1
	ds_bpermute_b32 v20, v51, v1
	s_waitcnt lgkmcnt(0)
	v_add_f32_e32 v1, v1, v20
	ds_bpermute_b32 v20, v162, v1
	s_waitcnt lgkmcnt(0)
	v_add_f32_e32 v1, v1, v20
	ds_bpermute_b32 v20, v163, v1
	s_waitcnt lgkmcnt(0)
	v_add_f32_e32 v1, v1, v20
	ds_bpermute_b32 v20, v164, v1
	s_waitcnt lgkmcnt(0)
	v_add_f32_e32 v1, v1, v20
	ds_bpermute_b32 v20, v165, v1
	s_waitcnt lgkmcnt(0)
	v_add_f32_e32 v1, v1, v20
	ds_bpermute_b32 v20, v166, v1
	s_waitcnt lgkmcnt(0)
	v_add_f32_e32 v1, v1, v20
	v_fmamk_f32 v1, v1, 0x3a000000, v223
	v_mul_f32_e32 v20, 0x4b800000, v1
	v_cmp_gt_f32_e32 vcc, s97, v1
	s_nop 1
	v_cndmask_b32_e32 v1, v1, v20, vcc
	v_rsq_f32_e32 v1, v1
	v_lshlrev_b64 v[20:21], 2, v[66:67]
	v_lshl_add_u64 v[36:37], v[56:57], 0, v[20:21]
	v_mul_f32_e32 v38, 0x45800000, v1
	v_cndmask_b32_e32 v38, v1, v38, vcc
	v_pk_mul_f32 v[40:41], v[100:101], v[38:39] op_sel_hi:[1,0]
	v_pk_mul_f32 v[42:43], v[110:111], v[38:39] op_sel_hi:[1,0]
	s_waitcnt vmcnt(0)
	v_pk_mul_f32 v[4:5], v[4:5], v[40:41]
	v_pk_mul_f32 v[6:7], v[6:7], v[42:43]
	global_store_dwordx4 v[36:37], v[4:7], off nt
	s_load_dwordx4 s[4:7], s[0:1], 0x90
	v_pk_mul_f32 v[10:11], v[10:11], v[38:39] op_sel_hi:[1,0]
	v_pk_mul_f32 v[8:9], v[8:9], v[38:39] op_sel_hi:[1,0]
	s_waitcnt lgkmcnt(0)
	s_movk_i32 s4, 0x1000
	v_lshl_add_u64 v[20:21], s[6:7], 0, v[20:21]
	v_lshl_add_u64 v[20:21], v[20:21], 0, v[2:3]
	v_pk_mul_f32 v[4:5], v[198:199], v[8:9]
	v_pk_mul_f32 v[6:7], v[200:201], v[10:11]
	global_store_dwordx4 v[20:21], v[4:7], off offset:1024 nt
	v_pk_mul_f32 v[8:9], v[14:15], v[38:39] op_sel_hi:[1,0]
	v_pk_mul_f32 v[10:11], v[12:13], v[38:39] op_sel_hi:[1,0]
	v_pk_mul_f32 v[12:13], v[18:19], v[38:39] op_sel_hi:[1,0]
	v_pk_mul_f32 v[4:5], v[202:203], v[10:11]
	v_pk_mul_f32 v[6:7], v[204:205], v[8:9]
	global_store_dwordx4 v[20:21], v[4:7], off offset:2048 nt
	v_pk_mul_f32 v[8:9], v[92:93], v[38:39] op_sel_hi:[1,0]
	v_pk_mul_f32 v[10:11], v[16:17], v[38:39] op_sel_hi:[1,0]
	v_pk_mul_f32 v[6:7], v[208:209], v[8:9]
	v_pk_mul_f32 v[4:5], v[206:207], v[10:11]
	global_store_dwordx4 v[20:21], v[4:7], off offset:3072 nt
	v_add_co_u32_e32 v8, vcc, s4, v20
	v_pk_mul_f32 v[10:11], v[22:23], v[38:39] op_sel_hi:[1,0]
	s_nop 0
	v_addc_co_u32_e32 v9, vcc, 0, v21, vcc
	v_cmp_lt_i32_e32 vcc, s73, v48
	s_or_b64 s[42:43], vcc, s[42:43]
	v_pk_mul_f32 v[4:5], v[210:211], v[12:13]
	v_pk_mul_f32 v[6:7], v[212:213], v[10:11]
	global_store_dwordx4 v[8:9], v[4:7], off nt
	v_pk_mul_f32 v[10:11], v[26:27], v[38:39] op_sel_hi:[1,0]
	v_pk_mul_f32 v[12:13], v[24:25], v[38:39] op_sel_hi:[1,0]
	v_pk_mul_f32 v[6:7], v[216:217], v[10:11]
	v_pk_mul_f32 v[4:5], v[214:215], v[12:13]
	global_store_dwordx4 v[8:9], v[4:7], off offset:1024 nt
	v_pk_mul_f32 v[10:11], v[30:31], v[38:39] op_sel_hi:[1,0]
	v_pk_mul_f32 v[12:13], v[28:29], v[38:39] op_sel_hi:[1,0]
	v_pk_mul_f32 v[6:7], v[220:221], v[10:11]
	v_pk_mul_f32 v[4:5], v[218:219], v[12:13]
	global_store_dwordx4 v[8:9], v[4:7], off offset:2048 nt
	v_pk_mul_f32 v[10:11], v[34:35], v[38:39] op_sel_hi:[1,0]
	v_pk_mul_f32 v[12:13], v[32:33], v[38:39] op_sel_hi:[1,0]
	v_pk_mul_f32 v[6:7], v[170:171], v[10:11]
	v_pk_mul_f32 v[4:5], v[168:169], v[12:13]
	global_store_dwordx4 v[8:9], v[4:7], off offset:3072 nt
	s_andn2_b64 exec, exec, s[42:43]
	s_cbranch_execz .LBB0_1896
